# ln1_router top-4 selection: branch-free compare/select chain, all 32 logits preloaded from LDS
# baseline (speedup 1.0000x reference)
.LBB0_1388:
	v_add_co_u32_e32 v8, vcc, 0x55664000, v48
	s_nop 1
	v_addc_co_u32_e32 v9, vcc, 0, v49, vcc
	v_add_co_u32_e32 v6, vcc, 0x55674000, v48
	s_nop 1
	v_addc_co_u32_e32 v7, vcc, 0, v49, vcc
	ds_read_b128 v[120:123], v10 offset:0
	global_load_dwordx4 v[56:59], v[8:9], off offset:2048
	global_load_dwordx4 v[88:91], v[6:7], off offset:2048
	ds_read_b128 v[124:127], v10 offset:64
	global_load_dwordx4 v[60:63], v[8:9], off offset:2112
	global_load_dwordx4 v[92:95], v[6:7], off offset:2112
	ds_read_b128 v[128:131], v10 offset:128
	global_load_dwordx4 v[64:67], v[8:9], off offset:2176
	global_load_dwordx4 v[96:99], v[6:7], off offset:2176
	ds_read_b128 v[132:135], v10 offset:192
	global_load_dwordx4 v[68:71], v[8:9], off offset:2240
	global_load_dwordx4 v[100:103], v[6:7], off offset:2240
	ds_read_b128 v[136:139], v10 offset:256
	global_load_dwordx4 v[72:75], v[8:9], off offset:2304
	global_load_dwordx4 v[104:107], v[6:7], off offset:2304
	ds_read_b128 v[140:143], v10 offset:320
	global_load_dwordx4 v[76:79], v[8:9], off offset:2368
	global_load_dwordx4 v[108:111], v[6:7], off offset:2368
	ds_read_b128 v[144:147], v10 offset:384
	global_load_dwordx4 v[80:83], v[8:9], off offset:2432
	global_load_dwordx4 v[112:115], v[6:7], off offset:2432
	ds_read_b128 v[148:151], v10 offset:448
	global_load_dwordx4 v[84:87], v[8:9], off offset:2496
	global_load_dwordx4 v[116:119], v[6:7], off offset:2496
	s_waitcnt vmcnt(15) lgkmcnt(7)
	v_mfma_f32_16x16x32_bf16 v[2:5], v[120:123], v[56:59], v[2:5]
	s_waitcnt vmcnt(14)
	v_mfma_f32_16x16x32_bf16 v[2:5], v[120:123], v[88:91], v[2:5]
	ds_read_b128 v[120:123], v10 offset:512
	global_load_dwordx4 v[56:59], v[8:9], off offset:2560
	global_load_dwordx4 v[88:91], v[6:7], off offset:2560
	s_waitcnt vmcnt(15) lgkmcnt(7)
	v_mfma_f32_16x16x32_bf16 v[2:5], v[124:127], v[60:63], v[2:5]
	s_waitcnt vmcnt(14)
	v_mfma_f32_16x16x32_bf16 v[2:5], v[124:127], v[92:95], v[2:5]
	ds_read_b128 v[124:127], v10 offset:576
	global_load_dwordx4 v[60:63], v[8:9], off offset:2624
	global_load_dwordx4 v[92:95], v[6:7], off offset:2624
	s_waitcnt vmcnt(15) lgkmcnt(7)
	v_mfma_f32_16x16x32_bf16 v[2:5], v[128:131], v[64:67], v[2:5]
	s_waitcnt vmcnt(14)
	v_mfma_f32_16x16x32_bf16 v[2:5], v[128:131], v[96:99], v[2:5]
	ds_read_b128 v[128:131], v10 offset:640
	global_load_dwordx4 v[64:67], v[8:9], off offset:2688
	global_load_dwordx4 v[96:99], v[6:7], off offset:2688
	s_waitcnt vmcnt(15) lgkmcnt(7)
	v_mfma_f32_16x16x32_bf16 v[2:5], v[132:135], v[68:71], v[2:5]
	s_waitcnt vmcnt(14)
	v_mfma_f32_16x16x32_bf16 v[2:5], v[132:135], v[100:103], v[2:5]
	ds_read_b128 v[132:135], v10 offset:704
	global_load_dwordx4 v[68:71], v[8:9], off offset:2752
	global_load_dwordx4 v[100:103], v[6:7], off offset:2752
	s_waitcnt vmcnt(15) lgkmcnt(7)
	v_mfma_f32_16x16x32_bf16 v[2:5], v[136:139], v[72:75], v[2:5]
	s_waitcnt vmcnt(14)
	v_mfma_f32_16x16x32_bf16 v[2:5], v[136:139], v[104:107], v[2:5]
	ds_read_b128 v[136:139], v10 offset:768
	global_load_dwordx4 v[72:75], v[8:9], off offset:2816
	global_load_dwordx4 v[104:107], v[6:7], off offset:2816
	s_waitcnt vmcnt(15) lgkmcnt(7)
	v_mfma_f32_16x16x32_bf16 v[2:5], v[140:143], v[76:79], v[2:5]
	s_waitcnt vmcnt(14)
	v_mfma_f32_16x16x32_bf16 v[2:5], v[140:143], v[108:111], v[2:5]
	ds_read_b128 v[140:143], v10 offset:832
	global_load_dwordx4 v[76:79], v[8:9], off offset:2880
	global_load_dwordx4 v[108:111], v[6:7], off offset:2880
	s_waitcnt vmcnt(15) lgkmcnt(7)
	v_mfma_f32_16x16x32_bf16 v[2:5], v[144:147], v[80:83], v[2:5]
	s_waitcnt vmcnt(14)
	v_mfma_f32_16x16x32_bf16 v[2:5], v[144:147], v[112:115], v[2:5]
	ds_read_b128 v[144:147], v10 offset:896
	global_load_dwordx4 v[80:83], v[8:9], off offset:2944
	global_load_dwordx4 v[112:115], v[6:7], off offset:2944
	s_waitcnt vmcnt(15) lgkmcnt(7)
	v_mfma_f32_16x16x32_bf16 v[2:5], v[148:151], v[84:87], v[2:5]
	s_waitcnt vmcnt(14)
	v_mfma_f32_16x16x32_bf16 v[2:5], v[148:151], v[116:119], v[2:5]
	ds_read_b128 v[148:151], v10 offset:960
	global_load_dwordx4 v[84:87], v[8:9], off offset:3008
	global_load_dwordx4 v[116:119], v[6:7], off offset:3008
	s_waitcnt vmcnt(15) lgkmcnt(7)
	v_mfma_f32_16x16x32_bf16 v[2:5], v[120:123], v[56:59], v[2:5]
	s_waitcnt vmcnt(14)
	v_mfma_f32_16x16x32_bf16 v[2:5], v[120:123], v[88:91], v[2:5]
	ds_read_b128 v[120:123], v10 offset:1024
	global_load_dwordx4 v[56:59], v[8:9], off offset:3072
	global_load_dwordx4 v[88:91], v[6:7], off offset:3072
	s_waitcnt vmcnt(15) lgkmcnt(7)
	v_mfma_f32_16x16x32_bf16 v[2:5], v[124:127], v[60:63], v[2:5]
	s_waitcnt vmcnt(14)
	v_mfma_f32_16x16x32_bf16 v[2:5], v[124:127], v[92:95], v[2:5]
	ds_read_b128 v[124:127], v10 offset:1088
	global_load_dwordx4 v[60:63], v[8:9], off offset:3136
	global_load_dwordx4 v[92:95], v[6:7], off offset:3136
	s_waitcnt vmcnt(15) lgkmcnt(7)
	v_mfma_f32_16x16x32_bf16 v[2:5], v[128:131], v[64:67], v[2:5]
	s_waitcnt vmcnt(14)
	v_mfma_f32_16x16x32_bf16 v[2:5], v[128:131], v[96:99], v[2:5]
	ds_read_b128 v[128:131], v10 offset:1152
	global_load_dwordx4 v[64:67], v[8:9], off offset:3200
	global_load_dwordx4 v[96:99], v[6:7], off offset:3200
	s_waitcnt vmcnt(15) lgkmcnt(7)
	v_mfma_f32_16x16x32_bf16 v[2:5], v[132:135], v[68:71], v[2:5]
	s_waitcnt vmcnt(14)
	v_mfma_f32_16x16x32_bf16 v[2:5], v[132:135], v[100:103], v[2:5]
	ds_read_b128 v[132:135], v10 offset:1216
	global_load_dwordx4 v[68:71], v[8:9], off offset:3264
	global_load_dwordx4 v[100:103], v[6:7], off offset:3264
	s_waitcnt vmcnt(15) lgkmcnt(7)
	v_mfma_f32_16x16x32_bf16 v[2:5], v[136:139], v[72:75], v[2:5]
	s_waitcnt vmcnt(14)
	v_mfma_f32_16x16x32_bf16 v[2:5], v[136:139], v[104:107], v[2:5]
	ds_read_b128 v[136:139], v10 offset:1280
	global_load_dwordx4 v[72:75], v[8:9], off offset:3328
	global_load_dwordx4 v[104:107], v[6:7], off offset:3328
	s_waitcnt vmcnt(15) lgkmcnt(7)
	v_mfma_f32_16x16x32_bf16 v[2:5], v[140:143], v[76:79], v[2:5]
	s_waitcnt vmcnt(14)
	v_mfma_f32_16x16x32_bf16 v[2:5], v[140:143], v[108:111], v[2:5]
	ds_read_b128 v[140:143], v10 offset:1344
	global_load_dwordx4 v[76:79], v[8:9], off offset:3392
	global_load_dwordx4 v[108:111], v[6:7], off offset:3392
	s_waitcnt vmcnt(15) lgkmcnt(7)
	v_mfma_f32_16x16x32_bf16 v[2:5], v[144:147], v[80:83], v[2:5]
	s_waitcnt vmcnt(14)
	v_mfma_f32_16x16x32_bf16 v[2:5], v[144:147], v[112:115], v[2:5]
	ds_read_b128 v[144:147], v10 offset:1408
	global_load_dwordx4 v[80:83], v[8:9], off offset:3456
	global_load_dwordx4 v[112:115], v[6:7], off offset:3456
	s_waitcnt vmcnt(15) lgkmcnt(7)
	v_mfma_f32_16x16x32_bf16 v[2:5], v[148:151], v[84:87], v[2:5]
	s_waitcnt vmcnt(14)
	v_mfma_f32_16x16x32_bf16 v[2:5], v[148:151], v[116:119], v[2:5]
	ds_read_b128 v[148:151], v10 offset:1472
	global_load_dwordx4 v[84:87], v[8:9], off offset:3520
	global_load_dwordx4 v[116:119], v[6:7], off offset:3520
	s_waitcnt vmcnt(15) lgkmcnt(7)
	v_mfma_f32_16x16x32_bf16 v[2:5], v[120:123], v[56:59], v[2:5]
	s_waitcnt vmcnt(14)
	v_mfma_f32_16x16x32_bf16 v[2:5], v[120:123], v[88:91], v[2:5]
	ds_read_b128 v[120:123], v10 offset:1536
	global_load_dwordx4 v[56:59], v[8:9], off offset:3584
	global_load_dwordx4 v[88:91], v[6:7], off offset:3584
	s_waitcnt vmcnt(15) lgkmcnt(7)
	v_mfma_f32_16x16x32_bf16 v[2:5], v[124:127], v[60:63], v[2:5]
	s_waitcnt vmcnt(14)
	v_mfma_f32_16x16x32_bf16 v[2:5], v[124:127], v[92:95], v[2:5]
	ds_read_b128 v[124:127], v10 offset:1600
	global_load_dwordx4 v[60:63], v[8:9], off offset:3648
	global_load_dwordx4 v[92:95], v[6:7], off offset:3648
	s_waitcnt vmcnt(15) lgkmcnt(7)
	v_mfma_f32_16x16x32_bf16 v[2:5], v[128:131], v[64:67], v[2:5]
	s_waitcnt vmcnt(14)
	v_mfma_f32_16x16x32_bf16 v[2:5], v[128:131], v[96:99], v[2:5]
	ds_read_b128 v[128:131], v10 offset:1664
	global_load_dwordx4 v[64:67], v[8:9], off offset:3712
	global_load_dwordx4 v[96:99], v[6:7], off offset:3712
	s_waitcnt vmcnt(15) lgkmcnt(7)
	v_mfma_f32_16x16x32_bf16 v[2:5], v[132:135], v[68:71], v[2:5]
	s_waitcnt vmcnt(14)
	v_mfma_f32_16x16x32_bf16 v[2:5], v[132:135], v[100:103], v[2:5]
	ds_read_b128 v[132:135], v10 offset:1728
	global_load_dwordx4 v[68:71], v[8:9], off offset:3776
	global_load_dwordx4 v[100:103], v[6:7], off offset:3776
	s_waitcnt vmcnt(15) lgkmcnt(7)
	v_mfma_f32_16x16x32_bf16 v[2:5], v[136:139], v[72:75], v[2:5]
	s_waitcnt vmcnt(14)
	v_mfma_f32_16x16x32_bf16 v[2:5], v[136:139], v[104:107], v[2:5]
	ds_read_b128 v[136:139], v10 offset:1792
	global_load_dwordx4 v[72:75], v[8:9], off offset:3840
	global_load_dwordx4 v[104:107], v[6:7], off offset:3840
	s_waitcnt vmcnt(15) lgkmcnt(7)
	v_mfma_f32_16x16x32_bf16 v[2:5], v[140:143], v[76:79], v[2:5]
	s_waitcnt vmcnt(14)
	v_mfma_f32_16x16x32_bf16 v[2:5], v[140:143], v[108:111], v[2:5]
	ds_read_b128 v[140:143], v10 offset:1856
	global_load_dwordx4 v[76:79], v[8:9], off offset:3904
	global_load_dwordx4 v[108:111], v[6:7], off offset:3904
	s_waitcnt vmcnt(15) lgkmcnt(7)
	v_mfma_f32_16x16x32_bf16 v[2:5], v[144:147], v[80:83], v[2:5]
	s_waitcnt vmcnt(14)
	v_mfma_f32_16x16x32_bf16 v[2:5], v[144:147], v[112:115], v[2:5]
	ds_read_b128 v[144:147], v10 offset:1920
	global_load_dwordx4 v[80:83], v[8:9], off offset:3968
	global_load_dwordx4 v[112:115], v[6:7], off offset:3968
	s_waitcnt vmcnt(15) lgkmcnt(7)
	v_mfma_f32_16x16x32_bf16 v[2:5], v[148:151], v[84:87], v[2:5]
	s_waitcnt vmcnt(14)
	v_mfma_f32_16x16x32_bf16 v[2:5], v[148:151], v[116:119], v[2:5]
	ds_read_b128 v[148:151], v10 offset:1984
	global_load_dwordx4 v[84:87], v[8:9], off offset:4032
	global_load_dwordx4 v[116:119], v[6:7], off offset:4032
	s_waitcnt vmcnt(15) lgkmcnt(7)
	v_mfma_f32_16x16x32_bf16 v[2:5], v[120:123], v[56:59], v[2:5]
	s_waitcnt vmcnt(14)
	v_mfma_f32_16x16x32_bf16 v[2:5], v[120:123], v[88:91], v[2:5]
	s_waitcnt vmcnt(13) lgkmcnt(6)
	v_mfma_f32_16x16x32_bf16 v[2:5], v[124:127], v[60:63], v[2:5]
	s_waitcnt vmcnt(12)
	v_mfma_f32_16x16x32_bf16 v[2:5], v[124:127], v[92:95], v[2:5]
	s_waitcnt vmcnt(11) lgkmcnt(5)
	v_mfma_f32_16x16x32_bf16 v[2:5], v[128:131], v[64:67], v[2:5]
	s_waitcnt vmcnt(10)
	v_mfma_f32_16x16x32_bf16 v[2:5], v[128:131], v[96:99], v[2:5]
	s_waitcnt vmcnt(9) lgkmcnt(4)
	v_mfma_f32_16x16x32_bf16 v[2:5], v[132:135], v[68:71], v[2:5]
	s_waitcnt vmcnt(8)
	v_mfma_f32_16x16x32_bf16 v[2:5], v[132:135], v[100:103], v[2:5]
	s_waitcnt vmcnt(7) lgkmcnt(3)
	v_mfma_f32_16x16x32_bf16 v[2:5], v[136:139], v[72:75], v[2:5]
	s_waitcnt vmcnt(6)
	v_mfma_f32_16x16x32_bf16 v[2:5], v[136:139], v[104:107], v[2:5]
	s_waitcnt vmcnt(5) lgkmcnt(2)
	v_mfma_f32_16x16x32_bf16 v[2:5], v[140:143], v[76:79], v[2:5]
	s_waitcnt vmcnt(4)
	v_mfma_f32_16x16x32_bf16 v[2:5], v[140:143], v[108:111], v[2:5]
	s_waitcnt vmcnt(3) lgkmcnt(1)
	v_mfma_f32_16x16x32_bf16 v[2:5], v[144:147], v[80:83], v[2:5]
	s_waitcnt vmcnt(2)
	v_mfma_f32_16x16x32_bf16 v[2:5], v[144:147], v[112:115], v[2:5]
	s_waitcnt vmcnt(1) lgkmcnt(0)
	v_mfma_f32_16x16x32_bf16 v[2:5], v[148:151], v[84:87], v[2:5]
	s_waitcnt vmcnt(0)
	v_mfma_f32_16x16x32_bf16 v[2:5], v[148:151], v[116:119], v[2:5]
	s_nop 0
	global_load_dword v6, v[38:39], off
	s_waitcnt vmcnt(0)
	s_nop 4
	v_add_f32_e32 v2, v2, v6
	v_add_f32_e32 v3, v3, v6
	v_add_f32_e32 v4, v4, v6
	v_add_f32_e32 v5, v5, v6
	ds_write2_b32 v196, v2, v3 offset1:33
	ds_write2_b32 v196, v4, v5 offset0:66 offset1:99
	s_waitcnt lgkmcnt(0)
	s_barrier
	s_and_saveexec_b64 s[0:1], s[14:15]
	s_cbranch_execz .LBB0_1765
	ds_read2_b32 v[56:57], v192 offset0:0 offset1:1
	ds_read2_b32 v[58:59], v192 offset0:2 offset1:3
	ds_read2_b32 v[60:61], v192 offset0:4 offset1:5
	ds_read2_b32 v[62:63], v192 offset0:6 offset1:7
	ds_read2_b32 v[64:65], v192 offset0:8 offset1:9
	ds_read2_b32 v[66:67], v192 offset0:10 offset1:11
	ds_read2_b32 v[68:69], v192 offset0:12 offset1:13
	ds_read2_b32 v[70:71], v192 offset0:14 offset1:15
	ds_read2_b32 v[72:73], v192 offset0:16 offset1:17
	ds_read2_b32 v[74:75], v192 offset0:18 offset1:19
	ds_read2_b32 v[76:77], v192 offset0:20 offset1:21
	ds_read2_b32 v[78:79], v192 offset0:22 offset1:23
	ds_read2_b32 v[80:81], v192 offset0:24 offset1:25
	ds_read2_b32 v[82:83], v192 offset0:26 offset1:27
	ds_read2_b32 v[84:85], v192 offset0:28 offset1:29
	ds_read2_b32 v[86:87], v192 offset0:30 offset1:31
	v_mov_b32_e32 v6, 0xff800000
	v_mov_b32_e32 v8, 0xff800000
	v_mov_b32_e32 v10, 0xff800000
	v_mov_b32_e32 v9, 0xff800000
	v_mov_b32_e32 v2, 0
	v_mov_b32_e32 v3, 0
	v_mov_b32_e32 v4, 0
	v_mov_b32_e32 v5, 0
	s_waitcnt lgkmcnt(15)
	v_cmp_gt_f32_e32 vcc, v56, v9
	v_cmp_gt_f32_e64 s[6:7], v56, v10
	v_cmp_gt_f32_e64 s[4:5], v56, v8
	v_cmp_gt_f32_e64 s[2:3], v56, v6
	v_cndmask_b32_e32 v9, v9, v56, vcc
	v_cndmask_b32_e64 v5, v5, 0, vcc
	v_cndmask_b32_e64 v9, v9, v10, s[6:7]
	v_cndmask_b32_e64 v5, v5, v4, s[6:7]
	v_cndmask_b32_e64 v10, v10, v56, s[6:7]
	v_cndmask_b32_e64 v4, v4, 0, s[6:7]
	v_cndmask_b32_e64 v10, v10, v8, s[4:5]
	v_cndmask_b32_e64 v4, v4, v3, s[4:5]
	v_cndmask_b32_e64 v8, v8, v56, s[4:5]
	v_cndmask_b32_e64 v3, v3, 0, s[4:5]
	v_cndmask_b32_e64 v8, v8, v6, s[2:3]
	v_cndmask_b32_e64 v3, v3, v2, s[2:3]
	v_cndmask_b32_e64 v6, v6, v56, s[2:3]
	v_cndmask_b32_e64 v2, v2, 0, s[2:3]
	v_cmp_gt_f32_e32 vcc, v57, v9
	v_cmp_gt_f32_e64 s[6:7], v57, v10
	v_cmp_gt_f32_e64 s[4:5], v57, v8
	v_cmp_gt_f32_e64 s[2:3], v57, v6
	v_cndmask_b32_e32 v9, v9, v57, vcc
	v_cndmask_b32_e64 v5, v5, 1, vcc
	v_cndmask_b32_e64 v9, v9, v10, s[6:7]
	v_cndmask_b32_e64 v5, v5, v4, s[6:7]
	v_cndmask_b32_e64 v10, v10, v57, s[6:7]
	v_cndmask_b32_e64 v4, v4, 1, s[6:7]
	v_cndmask_b32_e64 v10, v10, v8, s[4:5]
	v_cndmask_b32_e64 v4, v4, v3, s[4:5]
	v_cndmask_b32_e64 v8, v8, v57, s[4:5]
	v_cndmask_b32_e64 v3, v3, 1, s[4:5]
	v_cndmask_b32_e64 v8, v8, v6, s[2:3]
	v_cndmask_b32_e64 v3, v3, v2, s[2:3]
	v_cndmask_b32_e64 v6, v6, v57, s[2:3]
	v_cndmask_b32_e64 v2, v2, 1, s[2:3]
	s_waitcnt lgkmcnt(14)
	v_cmp_gt_f32_e32 vcc, v58, v9
	v_cmp_gt_f32_e64 s[6:7], v58, v10
	v_cmp_gt_f32_e64 s[4:5], v58, v8
	v_cmp_gt_f32_e64 s[2:3], v58, v6
	v_cndmask_b32_e32 v9, v9, v58, vcc
	v_cndmask_b32_e64 v5, v5, 2, vcc
	v_cndmask_b32_e64 v9, v9, v10, s[6:7]
	v_cndmask_b32_e64 v5, v5, v4, s[6:7]
	v_cndmask_b32_e64 v10, v10, v58, s[6:7]
	v_cndmask_b32_e64 v4, v4, 2, s[6:7]
	v_cndmask_b32_e64 v10, v10, v8, s[4:5]
	v_cndmask_b32_e64 v4, v4, v3, s[4:5]
	v_cndmask_b32_e64 v8, v8, v58, s[4:5]
	v_cndmask_b32_e64 v3, v3, 2, s[4:5]
	v_cndmask_b32_e64 v8, v8, v6, s[2:3]
	v_cndmask_b32_e64 v3, v3, v2, s[2:3]
	v_cndmask_b32_e64 v6, v6, v58, s[2:3]
	v_cndmask_b32_e64 v2, v2, 2, s[2:3]
	v_cmp_gt_f32_e32 vcc, v59, v9
	v_cmp_gt_f32_e64 s[6:7], v59, v10
	v_cmp_gt_f32_e64 s[4:5], v59, v8
	v_cmp_gt_f32_e64 s[2:3], v59, v6
	v_cndmask_b32_e32 v9, v9, v59, vcc
	v_cndmask_b32_e64 v5, v5, 3, vcc
	v_cndmask_b32_e64 v9, v9, v10, s[6:7]
	v_cndmask_b32_e64 v5, v5, v4, s[6:7]
	v_cndmask_b32_e64 v10, v10, v59, s[6:7]
	v_cndmask_b32_e64 v4, v4, 3, s[6:7]
	v_cndmask_b32_e64 v10, v10, v8, s[4:5]
	v_cndmask_b32_e64 v4, v4, v3, s[4:5]
	v_cndmask_b32_e64 v8, v8, v59, s[4:5]
	v_cndmask_b32_e64 v3, v3, 3, s[4:5]
	v_cndmask_b32_e64 v8, v8, v6, s[2:3]
	v_cndmask_b32_e64 v3, v3, v2, s[2:3]
	v_cndmask_b32_e64 v6, v6, v59, s[2:3]
	v_cndmask_b32_e64 v2, v2, 3, s[2:3]
	s_waitcnt lgkmcnt(13)
	v_cmp_gt_f32_e32 vcc, v60, v9
	v_cmp_gt_f32_e64 s[6:7], v60, v10
	v_cmp_gt_f32_e64 s[4:5], v60, v8
	v_cmp_gt_f32_e64 s[2:3], v60, v6
	v_cndmask_b32_e32 v9, v9, v60, vcc
	v_cndmask_b32_e64 v5, v5, 4, vcc
	v_cndmask_b32_e64 v9, v9, v10, s[6:7]
	v_cndmask_b32_e64 v5, v5, v4, s[6:7]
	v_cndmask_b32_e64 v10, v10, v60, s[6:7]
	v_cndmask_b32_e64 v4, v4, 4, s[6:7]
	v_cndmask_b32_e64 v10, v10, v8, s[4:5]
	v_cndmask_b32_e64 v4, v4, v3, s[4:5]
	v_cndmask_b32_e64 v8, v8, v60, s[4:5]
	v_cndmask_b32_e64 v3, v3, 4, s[4:5]
	v_cndmask_b32_e64 v8, v8, v6, s[2:3]
	v_cndmask_b32_e64 v3, v3, v2, s[2:3]
	v_cndmask_b32_e64 v6, v6, v60, s[2:3]
	v_cndmask_b32_e64 v2, v2, 4, s[2:3]
	v_cmp_gt_f32_e32 vcc, v61, v9
	v_cmp_gt_f32_e64 s[6:7], v61, v10
	v_cmp_gt_f32_e64 s[4:5], v61, v8
	v_cmp_gt_f32_e64 s[2:3], v61, v6
	v_cndmask_b32_e32 v9, v9, v61, vcc
	v_cndmask_b32_e64 v5, v5, 5, vcc
	v_cndmask_b32_e64 v9, v9, v10, s[6:7]
	v_cndmask_b32_e64 v5, v5, v4, s[6:7]
	v_cndmask_b32_e64 v10, v10, v61, s[6:7]
	v_cndmask_b32_e64 v4, v4, 5, s[6:7]
	v_cndmask_b32_e64 v10, v10, v8, s[4:5]
	v_cndmask_b32_e64 v4, v4, v3, s[4:5]
	v_cndmask_b32_e64 v8, v8, v61, s[4:5]
	v_cndmask_b32_e64 v3, v3, 5, s[4:5]
	v_cndmask_b32_e64 v8, v8, v6, s[2:3]
	v_cndmask_b32_e64 v3, v3, v2, s[2:3]
	v_cndmask_b32_e64 v6, v6, v61, s[2:3]
	v_cndmask_b32_e64 v2, v2, 5, s[2:3]
	s_waitcnt lgkmcnt(12)
	v_cmp_gt_f32_e32 vcc, v62, v9
	v_cmp_gt_f32_e64 s[6:7], v62, v10
	v_cmp_gt_f32_e64 s[4:5], v62, v8
	v_cmp_gt_f32_e64 s[2:3], v62, v6
	v_cndmask_b32_e32 v9, v9, v62, vcc
	v_cndmask_b32_e64 v5, v5, 6, vcc
	v_cndmask_b32_e64 v9, v9, v10, s[6:7]
	v_cndmask_b32_e64 v5, v5, v4, s[6:7]
	v_cndmask_b32_e64 v10, v10, v62, s[6:7]
	v_cndmask_b32_e64 v4, v4, 6, s[6:7]
	v_cndmask_b32_e64 v10, v10, v8, s[4:5]
	v_cndmask_b32_e64 v4, v4, v3, s[4:5]
	v_cndmask_b32_e64 v8, v8, v62, s[4:5]
	v_cndmask_b32_e64 v3, v3, 6, s[4:5]
	v_cndmask_b32_e64 v8, v8, v6, s[2:3]
	v_cndmask_b32_e64 v3, v3, v2, s[2:3]
	v_cndmask_b32_e64 v6, v6, v62, s[2:3]
	v_cndmask_b32_e64 v2, v2, 6, s[2:3]
	v_cmp_gt_f32_e32 vcc, v63, v9
	v_cmp_gt_f32_e64 s[6:7], v63, v10
	v_cmp_gt_f32_e64 s[4:5], v63, v8
	v_cmp_gt_f32_e64 s[2:3], v63, v6
	v_cndmask_b32_e32 v9, v9, v63, vcc
	v_cndmask_b32_e64 v5, v5, 7, vcc
	v_cndmask_b32_e64 v9, v9, v10, s[6:7]
	v_cndmask_b32_e64 v5, v5, v4, s[6:7]
	v_cndmask_b32_e64 v10, v10, v63, s[6:7]
	v_cndmask_b32_e64 v4, v4, 7, s[6:7]
	v_cndmask_b32_e64 v10, v10, v8, s[4:5]
	v_cndmask_b32_e64 v4, v4, v3, s[4:5]
	v_cndmask_b32_e64 v8, v8, v63, s[4:5]
	v_cndmask_b32_e64 v3, v3, 7, s[4:5]
	v_cndmask_b32_e64 v8, v8, v6, s[2:3]
	v_cndmask_b32_e64 v3, v3, v2, s[2:3]
	v_cndmask_b32_e64 v6, v6, v63, s[2:3]
	v_cndmask_b32_e64 v2, v2, 7, s[2:3]
	s_waitcnt lgkmcnt(11)
	v_cmp_gt_f32_e32 vcc, v64, v9
	v_cmp_gt_f32_e64 s[6:7], v64, v10
	v_cmp_gt_f32_e64 s[4:5], v64, v8
	v_cmp_gt_f32_e64 s[2:3], v64, v6
	v_cndmask_b32_e32 v9, v9, v64, vcc
	v_cndmask_b32_e64 v5, v5, 8, vcc
	v_cndmask_b32_e64 v9, v9, v10, s[6:7]
	v_cndmask_b32_e64 v5, v5, v4, s[6:7]
	v_cndmask_b32_e64 v10, v10, v64, s[6:7]
	v_cndmask_b32_e64 v4, v4, 8, s[6:7]
	v_cndmask_b32_e64 v10, v10, v8, s[4:5]
	v_cndmask_b32_e64 v4, v4, v3, s[4:5]
	v_cndmask_b32_e64 v8, v8, v64, s[4:5]
	v_cndmask_b32_e64 v3, v3, 8, s[4:5]
	v_cndmask_b32_e64 v8, v8, v6, s[2:3]
	v_cndmask_b32_e64 v3, v3, v2, s[2:3]
	v_cndmask_b32_e64 v6, v6, v64, s[2:3]
	v_cndmask_b32_e64 v2, v2, 8, s[2:3]
	v_cmp_gt_f32_e32 vcc, v65, v9
	v_cmp_gt_f32_e64 s[6:7], v65, v10
	v_cmp_gt_f32_e64 s[4:5], v65, v8
	v_cmp_gt_f32_e64 s[2:3], v65, v6
	v_cndmask_b32_e32 v9, v9, v65, vcc
	v_cndmask_b32_e64 v5, v5, 9, vcc
	v_cndmask_b32_e64 v9, v9, v10, s[6:7]
	v_cndmask_b32_e64 v5, v5, v4, s[6:7]
	v_cndmask_b32_e64 v10, v10, v65, s[6:7]
	v_cndmask_b32_e64 v4, v4, 9, s[6:7]
	v_cndmask_b32_e64 v10, v10, v8, s[4:5]
	v_cndmask_b32_e64 v4, v4, v3, s[4:5]
	v_cndmask_b32_e64 v8, v8, v65, s[4:5]
	v_cndmask_b32_e64 v3, v3, 9, s[4:5]
	v_cndmask_b32_e64 v8, v8, v6, s[2:3]
	v_cndmask_b32_e64 v3, v3, v2, s[2:3]
	v_cndmask_b32_e64 v6, v6, v65, s[2:3]
	v_cndmask_b32_e64 v2, v2, 9, s[2:3]
	s_waitcnt lgkmcnt(10)
	v_cmp_gt_f32_e32 vcc, v66, v9
	v_cmp_gt_f32_e64 s[6:7], v66, v10
	v_cmp_gt_f32_e64 s[4:5], v66, v8
	v_cmp_gt_f32_e64 s[2:3], v66, v6
	v_cndmask_b32_e32 v9, v9, v66, vcc
	v_cndmask_b32_e64 v5, v5, 10, vcc
	v_cndmask_b32_e64 v9, v9, v10, s[6:7]
	v_cndmask_b32_e64 v5, v5, v4, s[6:7]
	v_cndmask_b32_e64 v10, v10, v66, s[6:7]
	v_cndmask_b32_e64 v4, v4, 10, s[6:7]
	v_cndmask_b32_e64 v10, v10, v8, s[4:5]
	v_cndmask_b32_e64 v4, v4, v3, s[4:5]
	v_cndmask_b32_e64 v8, v8, v66, s[4:5]
	v_cndmask_b32_e64 v3, v3, 10, s[4:5]
	v_cndmask_b32_e64 v8, v8, v6, s[2:3]
	v_cndmask_b32_e64 v3, v3, v2, s[2:3]
	v_cndmask_b32_e64 v6, v6, v66, s[2:3]
	v_cndmask_b32_e64 v2, v2, 10, s[2:3]
	v_cmp_gt_f32_e32 vcc, v67, v9
	v_cmp_gt_f32_e64 s[6:7], v67, v10
	v_cmp_gt_f32_e64 s[4:5], v67, v8
	v_cmp_gt_f32_e64 s[2:3], v67, v6
	v_cndmask_b32_e32 v9, v9, v67, vcc
	v_cndmask_b32_e64 v5, v5, 11, vcc
	v_cndmask_b32_e64 v9, v9, v10, s[6:7]
	v_cndmask_b32_e64 v5, v5, v4, s[6:7]
	v_cndmask_b32_e64 v10, v10, v67, s[6:7]
	v_cndmask_b32_e64 v4, v4, 11, s[6:7]
	v_cndmask_b32_e64 v10, v10, v8, s[4:5]
	v_cndmask_b32_e64 v4, v4, v3, s[4:5]
	v_cndmask_b32_e64 v8, v8, v67, s[4:5]
	v_cndmask_b32_e64 v3, v3, 11, s[4:5]
	v_cndmask_b32_e64 v8, v8, v6, s[2:3]
	v_cndmask_b32_e64 v3, v3, v2, s[2:3]
	v_cndmask_b32_e64 v6, v6, v67, s[2:3]
	v_cndmask_b32_e64 v2, v2, 11, s[2:3]
	s_waitcnt lgkmcnt(9)
	v_cmp_gt_f32_e32 vcc, v68, v9
	v_cmp_gt_f32_e64 s[6:7], v68, v10
	v_cmp_gt_f32_e64 s[4:5], v68, v8
	v_cmp_gt_f32_e64 s[2:3], v68, v6
	v_cndmask_b32_e32 v9, v9, v68, vcc
	v_cndmask_b32_e64 v5, v5, 12, vcc
	v_cndmask_b32_e64 v9, v9, v10, s[6:7]
	v_cndmask_b32_e64 v5, v5, v4, s[6:7]
	v_cndmask_b32_e64 v10, v10, v68, s[6:7]
	v_cndmask_b32_e64 v4, v4, 12, s[6:7]
	v_cndmask_b32_e64 v10, v10, v8, s[4:5]
	v_cndmask_b32_e64 v4, v4, v3, s[4:5]
	v_cndmask_b32_e64 v8, v8, v68, s[4:5]
	v_cndmask_b32_e64 v3, v3, 12, s[4:5]
	v_cndmask_b32_e64 v8, v8, v6, s[2:3]
	v_cndmask_b32_e64 v3, v3, v2, s[2:3]
	v_cndmask_b32_e64 v6, v6, v68, s[2:3]
	v_cndmask_b32_e64 v2, v2, 12, s[2:3]
	v_cmp_gt_f32_e32 vcc, v69, v9
	v_cmp_gt_f32_e64 s[6:7], v69, v10
	v_cmp_gt_f32_e64 s[4:5], v69, v8
	v_cmp_gt_f32_e64 s[2:3], v69, v6
	v_cndmask_b32_e32 v9, v9, v69, vcc
	v_cndmask_b32_e64 v5, v5, 13, vcc
	v_cndmask_b32_e64 v9, v9, v10, s[6:7]
	v_cndmask_b32_e64 v5, v5, v4, s[6:7]
	v_cndmask_b32_e64 v10, v10, v69, s[6:7]
	v_cndmask_b32_e64 v4, v4, 13, s[6:7]
	v_cndmask_b32_e64 v10, v10, v8, s[4:5]
	v_cndmask_b32_e64 v4, v4, v3, s[4:5]
	v_cndmask_b32_e64 v8, v8, v69, s[4:5]
	v_cndmask_b32_e64 v3, v3, 13, s[4:5]
	v_cndmask_b32_e64 v8, v8, v6, s[2:3]
	v_cndmask_b32_e64 v3, v3, v2, s[2:3]
	v_cndmask_b32_e64 v6, v6, v69, s[2:3]
	v_cndmask_b32_e64 v2, v2, 13, s[2:3]
	s_waitcnt lgkmcnt(8)
	v_cmp_gt_f32_e32 vcc, v70, v9
	v_cmp_gt_f32_e64 s[6:7], v70, v10
	v_cmp_gt_f32_e64 s[4:5], v70, v8
	v_cmp_gt_f32_e64 s[2:3], v70, v6
	v_cndmask_b32_e32 v9, v9, v70, vcc
	v_cndmask_b32_e64 v5, v5, 14, vcc
	v_cndmask_b32_e64 v9, v9, v10, s[6:7]
	v_cndmask_b32_e64 v5, v5, v4, s[6:7]
	v_cndmask_b32_e64 v10, v10, v70, s[6:7]
	v_cndmask_b32_e64 v4, v4, 14, s[6:7]
	v_cndmask_b32_e64 v10, v10, v8, s[4:5]
	v_cndmask_b32_e64 v4, v4, v3, s[4:5]
	v_cndmask_b32_e64 v8, v8, v70, s[4:5]
	v_cndmask_b32_e64 v3, v3, 14, s[4:5]
	v_cndmask_b32_e64 v8, v8, v6, s[2:3]
	v_cndmask_b32_e64 v3, v3, v2, s[2:3]
	v_cndmask_b32_e64 v6, v6, v70, s[2:3]
	v_cndmask_b32_e64 v2, v2, 14, s[2:3]
	v_cmp_gt_f32_e32 vcc, v71, v9
	v_cmp_gt_f32_e64 s[6:7], v71, v10
	v_cmp_gt_f32_e64 s[4:5], v71, v8
	v_cmp_gt_f32_e64 s[2:3], v71, v6
	v_cndmask_b32_e32 v9, v9, v71, vcc
	v_cndmask_b32_e64 v5, v5, 15, vcc
	v_cndmask_b32_e64 v9, v9, v10, s[6:7]
	v_cndmask_b32_e64 v5, v5, v4, s[6:7]
	v_cndmask_b32_e64 v10, v10, v71, s[6:7]
	v_cndmask_b32_e64 v4, v4, 15, s[6:7]
	v_cndmask_b32_e64 v10, v10, v8, s[4:5]
	v_cndmask_b32_e64 v4, v4, v3, s[4:5]
	v_cndmask_b32_e64 v8, v8, v71, s[4:5]
	v_cndmask_b32_e64 v3, v3, 15, s[4:5]
	v_cndmask_b32_e64 v8, v8, v6, s[2:3]
	v_cndmask_b32_e64 v3, v3, v2, s[2:3]
	v_cndmask_b32_e64 v6, v6, v71, s[2:3]
	v_cndmask_b32_e64 v2, v2, 15, s[2:3]
	s_waitcnt lgkmcnt(7)
	v_cmp_gt_f32_e32 vcc, v72, v9
	v_cmp_gt_f32_e64 s[6:7], v72, v10
	v_cmp_gt_f32_e64 s[4:5], v72, v8
	v_cmp_gt_f32_e64 s[2:3], v72, v6
	v_cndmask_b32_e32 v9, v9, v72, vcc
	v_cndmask_b32_e64 v5, v5, 16, vcc
	v_cndmask_b32_e64 v9, v9, v10, s[6:7]
	v_cndmask_b32_e64 v5, v5, v4, s[6:7]
	v_cndmask_b32_e64 v10, v10, v72, s[6:7]
	v_cndmask_b32_e64 v4, v4, 16, s[6:7]
	v_cndmask_b32_e64 v10, v10, v8, s[4:5]
	v_cndmask_b32_e64 v4, v4, v3, s[4:5]
	v_cndmask_b32_e64 v8, v8, v72, s[4:5]
	v_cndmask_b32_e64 v3, v3, 16, s[4:5]
	v_cndmask_b32_e64 v8, v8, v6, s[2:3]
	v_cndmask_b32_e64 v3, v3, v2, s[2:3]
	v_cndmask_b32_e64 v6, v6, v72, s[2:3]
	v_cndmask_b32_e64 v2, v2, 16, s[2:3]
	v_cmp_gt_f32_e32 vcc, v73, v9
	v_cmp_gt_f32_e64 s[6:7], v73, v10
	v_cmp_gt_f32_e64 s[4:5], v73, v8
	v_cmp_gt_f32_e64 s[2:3], v73, v6
	v_cndmask_b32_e32 v9, v9, v73, vcc
	v_cndmask_b32_e64 v5, v5, 17, vcc
	v_cndmask_b32_e64 v9, v9, v10, s[6:7]
	v_cndmask_b32_e64 v5, v5, v4, s[6:7]
	v_cndmask_b32_e64 v10, v10, v73, s[6:7]
	v_cndmask_b32_e64 v4, v4, 17, s[6:7]
	v_cndmask_b32_e64 v10, v10, v8, s[4:5]
	v_cndmask_b32_e64 v4, v4, v3, s[4:5]
	v_cndmask_b32_e64 v8, v8, v73, s[4:5]
	v_cndmask_b32_e64 v3, v3, 17, s[4:5]
	v_cndmask_b32_e64 v8, v8, v6, s[2:3]
	v_cndmask_b32_e64 v3, v3, v2, s[2:3]
	v_cndmask_b32_e64 v6, v6, v73, s[2:3]
	v_cndmask_b32_e64 v2, v2, 17, s[2:3]
	s_waitcnt lgkmcnt(6)
	v_cmp_gt_f32_e32 vcc, v74, v9
	v_cmp_gt_f32_e64 s[6:7], v74, v10
	v_cmp_gt_f32_e64 s[4:5], v74, v8
	v_cmp_gt_f32_e64 s[2:3], v74, v6
	v_cndmask_b32_e32 v9, v9, v74, vcc
	v_cndmask_b32_e64 v5, v5, 18, vcc
	v_cndmask_b32_e64 v9, v9, v10, s[6:7]
	v_cndmask_b32_e64 v5, v5, v4, s[6:7]
	v_cndmask_b32_e64 v10, v10, v74, s[6:7]
	v_cndmask_b32_e64 v4, v4, 18, s[6:7]
	v_cndmask_b32_e64 v10, v10, v8, s[4:5]
	v_cndmask_b32_e64 v4, v4, v3, s[4:5]
	v_cndmask_b32_e64 v8, v8, v74, s[4:5]
	v_cndmask_b32_e64 v3, v3, 18, s[4:5]
	v_cndmask_b32_e64 v8, v8, v6, s[2:3]
	v_cndmask_b32_e64 v3, v3, v2, s[2:3]
	v_cndmask_b32_e64 v6, v6, v74, s[2:3]
	v_cndmask_b32_e64 v2, v2, 18, s[2:3]
	v_cmp_gt_f32_e32 vcc, v75, v9
	v_cmp_gt_f32_e64 s[6:7], v75, v10
	v_cmp_gt_f32_e64 s[4:5], v75, v8
	v_cmp_gt_f32_e64 s[2:3], v75, v6
	v_cndmask_b32_e32 v9, v9, v75, vcc
	v_cndmask_b32_e64 v5, v5, 19, vcc
	v_cndmask_b32_e64 v9, v9, v10, s[6:7]
	v_cndmask_b32_e64 v5, v5, v4, s[6:7]
	v_cndmask_b32_e64 v10, v10, v75, s[6:7]
	v_cndmask_b32_e64 v4, v4, 19, s[6:7]
	v_cndmask_b32_e64 v10, v10, v8, s[4:5]
	v_cndmask_b32_e64 v4, v4, v3, s[4:5]
	v_cndmask_b32_e64 v8, v8, v75, s[4:5]
	v_cndmask_b32_e64 v3, v3, 19, s[4:5]
	v_cndmask_b32_e64 v8, v8, v6, s[2:3]
	v_cndmask_b32_e64 v3, v3, v2, s[2:3]
	v_cndmask_b32_e64 v6, v6, v75, s[2:3]
	v_cndmask_b32_e64 v2, v2, 19, s[2:3]
	s_waitcnt lgkmcnt(5)
	v_cmp_gt_f32_e32 vcc, v76, v9
	v_cmp_gt_f32_e64 s[6:7], v76, v10
	v_cmp_gt_f32_e64 s[4:5], v76, v8
	v_cmp_gt_f32_e64 s[2:3], v76, v6
	v_cndmask_b32_e32 v9, v9, v76, vcc
	v_cndmask_b32_e64 v5, v5, 20, vcc
	v_cndmask_b32_e64 v9, v9, v10, s[6:7]
	v_cndmask_b32_e64 v5, v5, v4, s[6:7]
	v_cndmask_b32_e64 v10, v10, v76, s[6:7]
	v_cndmask_b32_e64 v4, v4, 20, s[6:7]
	v_cndmask_b32_e64 v10, v10, v8, s[4:5]
	v_cndmask_b32_e64 v4, v4, v3, s[4:5]
	v_cndmask_b32_e64 v8, v8, v76, s[4:5]
	v_cndmask_b32_e64 v3, v3, 20, s[4:5]
	v_cndmask_b32_e64 v8, v8, v6, s[2:3]
	v_cndmask_b32_e64 v3, v3, v2, s[2:3]
	v_cndmask_b32_e64 v6, v6, v76, s[2:3]
	v_cndmask_b32_e64 v2, v2, 20, s[2:3]
	v_cmp_gt_f32_e32 vcc, v77, v9
	v_cmp_gt_f32_e64 s[6:7], v77, v10
	v_cmp_gt_f32_e64 s[4:5], v77, v8
	v_cmp_gt_f32_e64 s[2:3], v77, v6
	v_cndmask_b32_e32 v9, v9, v77, vcc
	v_cndmask_b32_e64 v5, v5, 21, vcc
	v_cndmask_b32_e64 v9, v9, v10, s[6:7]
	v_cndmask_b32_e64 v5, v5, v4, s[6:7]
	v_cndmask_b32_e64 v10, v10, v77, s[6:7]
	v_cndmask_b32_e64 v4, v4, 21, s[6:7]
	v_cndmask_b32_e64 v10, v10, v8, s[4:5]
	v_cndmask_b32_e64 v4, v4, v3, s[4:5]
	v_cndmask_b32_e64 v8, v8, v77, s[4:5]
	v_cndmask_b32_e64 v3, v3, 21, s[4:5]
	v_cndmask_b32_e64 v8, v8, v6, s[2:3]
	v_cndmask_b32_e64 v3, v3, v2, s[2:3]
	v_cndmask_b32_e64 v6, v6, v77, s[2:3]
	v_cndmask_b32_e64 v2, v2, 21, s[2:3]
	s_waitcnt lgkmcnt(4)
	v_cmp_gt_f32_e32 vcc, v78, v9
	v_cmp_gt_f32_e64 s[6:7], v78, v10
	v_cmp_gt_f32_e64 s[4:5], v78, v8
	v_cmp_gt_f32_e64 s[2:3], v78, v6
	v_cndmask_b32_e32 v9, v9, v78, vcc
	v_cndmask_b32_e64 v5, v5, 22, vcc
	v_cndmask_b32_e64 v9, v9, v10, s[6:7]
	v_cndmask_b32_e64 v5, v5, v4, s[6:7]
	v_cndmask_b32_e64 v10, v10, v78, s[6:7]
	v_cndmask_b32_e64 v4, v4, 22, s[6:7]
	v_cndmask_b32_e64 v10, v10, v8, s[4:5]
	v_cndmask_b32_e64 v4, v4, v3, s[4:5]
	v_cndmask_b32_e64 v8, v8, v78, s[4:5]
	v_cndmask_b32_e64 v3, v3, 22, s[4:5]
	v_cndmask_b32_e64 v8, v8, v6, s[2:3]
	v_cndmask_b32_e64 v3, v3, v2, s[2:3]
	v_cndmask_b32_e64 v6, v6, v78, s[2:3]
	v_cndmask_b32_e64 v2, v2, 22, s[2:3]
	v_cmp_gt_f32_e32 vcc, v79, v9
	v_cmp_gt_f32_e64 s[6:7], v79, v10
	v_cmp_gt_f32_e64 s[4:5], v79, v8
	v_cmp_gt_f32_e64 s[2:3], v79, v6
	v_cndmask_b32_e32 v9, v9, v79, vcc
	v_cndmask_b32_e64 v5, v5, 23, vcc
	v_cndmask_b32_e64 v9, v9, v10, s[6:7]
	v_cndmask_b32_e64 v5, v5, v4, s[6:7]
	v_cndmask_b32_e64 v10, v10, v79, s[6:7]
	v_cndmask_b32_e64 v4, v4, 23, s[6:7]
	v_cndmask_b32_e64 v10, v10, v8, s[4:5]
	v_cndmask_b32_e64 v4, v4, v3, s[4:5]
	v_cndmask_b32_e64 v8, v8, v79, s[4:5]
	v_cndmask_b32_e64 v3, v3, 23, s[4:5]
	v_cndmask_b32_e64 v8, v8, v6, s[2:3]
	v_cndmask_b32_e64 v3, v3, v2, s[2:3]
	v_cndmask_b32_e64 v6, v6, v79, s[2:3]
	v_cndmask_b32_e64 v2, v2, 23, s[2:3]
	s_waitcnt lgkmcnt(3)
	v_cmp_gt_f32_e32 vcc, v80, v9
	v_cmp_gt_f32_e64 s[6:7], v80, v10
	v_cmp_gt_f32_e64 s[4:5], v80, v8
	v_cmp_gt_f32_e64 s[2:3], v80, v6
	v_cndmask_b32_e32 v9, v9, v80, vcc
	v_cndmask_b32_e64 v5, v5, 24, vcc
	v_cndmask_b32_e64 v9, v9, v10, s[6:7]
	v_cndmask_b32_e64 v5, v5, v4, s[6:7]
	v_cndmask_b32_e64 v10, v10, v80, s[6:7]
	v_cndmask_b32_e64 v4, v4, 24, s[6:7]
	v_cndmask_b32_e64 v10, v10, v8, s[4:5]
	v_cndmask_b32_e64 v4, v4, v3, s[4:5]
	v_cndmask_b32_e64 v8, v8, v80, s[4:5]
	v_cndmask_b32_e64 v3, v3, 24, s[4:5]
	v_cndmask_b32_e64 v8, v8, v6, s[2:3]
	v_cndmask_b32_e64 v3, v3, v2, s[2:3]
	v_cndmask_b32_e64 v6, v6, v80, s[2:3]
	v_cndmask_b32_e64 v2, v2, 24, s[2:3]
	v_cmp_gt_f32_e32 vcc, v81, v9
	v_cmp_gt_f32_e64 s[6:7], v81, v10
	v_cmp_gt_f32_e64 s[4:5], v81, v8
	v_cmp_gt_f32_e64 s[2:3], v81, v6
	v_cndmask_b32_e32 v9, v9, v81, vcc
	v_cndmask_b32_e64 v5, v5, 25, vcc
	v_cndmask_b32_e64 v9, v9, v10, s[6:7]
	v_cndmask_b32_e64 v5, v5, v4, s[6:7]
	v_cndmask_b32_e64 v10, v10, v81, s[6:7]
	v_cndmask_b32_e64 v4, v4, 25, s[6:7]
	v_cndmask_b32_e64 v10, v10, v8, s[4:5]
	v_cndmask_b32_e64 v4, v4, v3, s[4:5]
	v_cndmask_b32_e64 v8, v8, v81, s[4:5]
	v_cndmask_b32_e64 v3, v3, 25, s[4:5]
	v_cndmask_b32_e64 v8, v8, v6, s[2:3]
	v_cndmask_b32_e64 v3, v3, v2, s[2:3]
	v_cndmask_b32_e64 v6, v6, v81, s[2:3]
	v_cndmask_b32_e64 v2, v2, 25, s[2:3]
	s_waitcnt lgkmcnt(2)
	v_cmp_gt_f32_e32 vcc, v82, v9
	v_cmp_gt_f32_e64 s[6:7], v82, v10
	v_cmp_gt_f32_e64 s[4:5], v82, v8
	v_cmp_gt_f32_e64 s[2:3], v82, v6
	v_cndmask_b32_e32 v9, v9, v82, vcc
	v_cndmask_b32_e64 v5, v5, 26, vcc
	v_cndmask_b32_e64 v9, v9, v10, s[6:7]
	v_cndmask_b32_e64 v5, v5, v4, s[6:7]
	v_cndmask_b32_e64 v10, v10, v82, s[6:7]
	v_cndmask_b32_e64 v4, v4, 26, s[6:7]
	v_cndmask_b32_e64 v10, v10, v8, s[4:5]
	v_cndmask_b32_e64 v4, v4, v3, s[4:5]
	v_cndmask_b32_e64 v8, v8, v82, s[4:5]
	v_cndmask_b32_e64 v3, v3, 26, s[4:5]
	v_cndmask_b32_e64 v8, v8, v6, s[2:3]
	v_cndmask_b32_e64 v3, v3, v2, s[2:3]
	v_cndmask_b32_e64 v6, v6, v82, s[2:3]
	v_cndmask_b32_e64 v2, v2, 26, s[2:3]
	v_cmp_gt_f32_e32 vcc, v83, v9
	v_cmp_gt_f32_e64 s[6:7], v83, v10
	v_cmp_gt_f32_e64 s[4:5], v83, v8
	v_cmp_gt_f32_e64 s[2:3], v83, v6
	v_cndmask_b32_e32 v9, v9, v83, vcc
	v_cndmask_b32_e64 v5, v5, 27, vcc
	v_cndmask_b32_e64 v9, v9, v10, s[6:7]
	v_cndmask_b32_e64 v5, v5, v4, s[6:7]
	v_cndmask_b32_e64 v10, v10, v83, s[6:7]
	v_cndmask_b32_e64 v4, v4, 27, s[6:7]
	v_cndmask_b32_e64 v10, v10, v8, s[4:5]
	v_cndmask_b32_e64 v4, v4, v3, s[4:5]
	v_cndmask_b32_e64 v8, v8, v83, s[4:5]
	v_cndmask_b32_e64 v3, v3, 27, s[4:5]
	v_cndmask_b32_e64 v8, v8, v6, s[2:3]
	v_cndmask_b32_e64 v3, v3, v2, s[2:3]
	v_cndmask_b32_e64 v6, v6, v83, s[2:3]
	v_cndmask_b32_e64 v2, v2, 27, s[2:3]
	s_waitcnt lgkmcnt(1)
	v_cmp_gt_f32_e32 vcc, v84, v9
	v_cmp_gt_f32_e64 s[6:7], v84, v10
	v_cmp_gt_f32_e64 s[4:5], v84, v8
	v_cmp_gt_f32_e64 s[2:3], v84, v6
	v_cndmask_b32_e32 v9, v9, v84, vcc
	v_cndmask_b32_e64 v5, v5, 28, vcc
	v_cndmask_b32_e64 v9, v9, v10, s[6:7]
	v_cndmask_b32_e64 v5, v5, v4, s[6:7]
	v_cndmask_b32_e64 v10, v10, v84, s[6:7]
	v_cndmask_b32_e64 v4, v4, 28, s[6:7]
	v_cndmask_b32_e64 v10, v10, v8, s[4:5]
	v_cndmask_b32_e64 v4, v4, v3, s[4:5]
	v_cndmask_b32_e64 v8, v8, v84, s[4:5]
	v_cndmask_b32_e64 v3, v3, 28, s[4:5]
	v_cndmask_b32_e64 v8, v8, v6, s[2:3]
	v_cndmask_b32_e64 v3, v3, v2, s[2:3]
	v_cndmask_b32_e64 v6, v6, v84, s[2:3]
	v_cndmask_b32_e64 v2, v2, 28, s[2:3]
	v_cmp_gt_f32_e32 vcc, v85, v9
	v_cmp_gt_f32_e64 s[6:7], v85, v10
	v_cmp_gt_f32_e64 s[4:5], v85, v8
	v_cmp_gt_f32_e64 s[2:3], v85, v6
	v_cndmask_b32_e32 v9, v9, v85, vcc
	v_cndmask_b32_e64 v5, v5, 29, vcc
	v_cndmask_b32_e64 v9, v9, v10, s[6:7]
	v_cndmask_b32_e64 v5, v5, v4, s[6:7]
	v_cndmask_b32_e64 v10, v10, v85, s[6:7]
	v_cndmask_b32_e64 v4, v4, 29, s[6:7]
	v_cndmask_b32_e64 v10, v10, v8, s[4:5]
	v_cndmask_b32_e64 v4, v4, v3, s[4:5]
	v_cndmask_b32_e64 v8, v8, v85, s[4:5]
	v_cndmask_b32_e64 v3, v3, 29, s[4:5]
	v_cndmask_b32_e64 v8, v8, v6, s[2:3]
	v_cndmask_b32_e64 v3, v3, v2, s[2:3]
	v_cndmask_b32_e64 v6, v6, v85, s[2:3]
	v_cndmask_b32_e64 v2, v2, 29, s[2:3]
	s_waitcnt lgkmcnt(0)
	v_cmp_gt_f32_e32 vcc, v86, v9
	v_cmp_gt_f32_e64 s[6:7], v86, v10
	v_cmp_gt_f32_e64 s[4:5], v86, v8
	v_cmp_gt_f32_e64 s[2:3], v86, v6
	v_cndmask_b32_e32 v9, v9, v86, vcc
	v_cndmask_b32_e64 v5, v5, 30, vcc
	v_cndmask_b32_e64 v9, v9, v10, s[6:7]
	v_cndmask_b32_e64 v5, v5, v4, s[6:7]
	v_cndmask_b32_e64 v10, v10, v86, s[6:7]
	v_cndmask_b32_e64 v4, v4, 30, s[6:7]
	v_cndmask_b32_e64 v10, v10, v8, s[4:5]
	v_cndmask_b32_e64 v4, v4, v3, s[4:5]
	v_cndmask_b32_e64 v8, v8, v86, s[4:5]
	v_cndmask_b32_e64 v3, v3, 30, s[4:5]
	v_cndmask_b32_e64 v8, v8, v6, s[2:3]
	v_cndmask_b32_e64 v3, v3, v2, s[2:3]
	v_cndmask_b32_e64 v6, v6, v86, s[2:3]
	v_cndmask_b32_e64 v2, v2, 30, s[2:3]
	v_cmp_gt_f32_e32 vcc, v87, v9
	v_cmp_gt_f32_e64 s[6:7], v87, v10
	v_cmp_gt_f32_e64 s[4:5], v87, v8
	v_cmp_gt_f32_e64 s[2:3], v87, v6
	v_cndmask_b32_e32 v9, v9, v87, vcc
	v_cndmask_b32_e64 v5, v5, 31, vcc
	v_cndmask_b32_e64 v9, v9, v10, s[6:7]
	v_cndmask_b32_e64 v5, v5, v4, s[6:7]
	v_cndmask_b32_e64 v10, v10, v87, s[6:7]
	v_cndmask_b32_e64 v4, v4, 31, s[6:7]
	v_cndmask_b32_e64 v10, v10, v8, s[4:5]
	v_cndmask_b32_e64 v4, v4, v3, s[4:5]
	v_cndmask_b32_e64 v8, v8, v87, s[4:5]
	v_cndmask_b32_e64 v3, v3, 31, s[4:5]
	v_cndmask_b32_e64 v8, v8, v6, s[2:3]
	v_cndmask_b32_e64 v3, v3, v2, s[2:3]
	v_cndmask_b32_e64 v6, v6, v87, s[2:3]
	v_cndmask_b32_e64 v2, v2, 31, s[2:3]
	s_mov_b64 s[2:3], exec
